# baseline (speedup 1.0000x reference)
.Lwo_ni_a:
.LBB3_16:
	v_max_f32_e32 v36, 0xf149f2ca, v2
	v_cndmask_b32_e64 v194, v36, v217, s[0:1]
	v_mul_f32_e32 v2, 0xbe0293ee, v194
	v_fmamk_f32 v20, v20, 0x3e0293ee, v2
	v_exp_f32_e32 v143, v20
	v_sub_f32_e32 v20, 0xf149f2ca, v36
	v_mul_f32_e32 v20, 0x3e0293ee, v20
	v_fmamk_f32 v21, v21, 0x3e0293ee, v2
	v_fmamk_f32 v22, v22, 0x3e0293ee, v2
	v_fmamk_f32 v23, v23, 0x3e0293ee, v2
	v_fmamk_f32 v24, v24, 0x3e0293ee, v2
	v_fmamk_f32 v25, v25, 0x3e0293ee, v2
	v_fmamk_f32 v26, v26, 0x3e0293ee, v2
	v_fmamk_f32 v27, v27, 0x3e0293ee, v2
	v_fmamk_f32 v28, v28, 0x3e0293ee, v2
	v_fmamk_f32 v29, v29, 0x3e0293ee, v2
	v_fmamk_f32 v30, v30, 0x3e0293ee, v2
	v_fmamk_f32 v31, v31, 0x3e0293ee, v2
	v_fmamk_f32 v32, v32, 0x3e0293ee, v2
	v_fmamk_f32 v33, v33, 0x3e0293ee, v2
	v_fmamk_f32 v34, v34, 0x3e0293ee, v2
	v_fmamk_f32 v35, v35, 0x3e0293ee, v2
	v_exp_f32_e32 v20, v20
	v_exp_f32_e32 v145, v21
	v_exp_f32_e32 v141, v22
	v_exp_f32_e32 v144, v23
	v_exp_f32_e32 v140, v24
	v_exp_f32_e32 v142, v25
	v_exp_f32_e32 v138, v26
	v_exp_f32_e32 v139, v27
	v_exp_f32_e32 v133, v28
	v_exp_f32_e32 v136, v29
	v_exp_f32_e32 v131, v30
	v_exp_f32_e32 v134, v31
	v_exp_f32_e32 v130, v32
	v_exp_f32_e32 v137, v33
	v_exp_f32_e32 v132, v34
	v_exp_f32_e32 v135, v35
	v_cndmask_b32_e64 v219, v20, 1.0, s[0:1]
	v_fma_f32 v128, v18, s18, v2
	v_fma_f32 v129, v19, s18, v2
	v_fma_f32 v126, v16, s18, v2
	v_fma_f32 v127, v17, s18, v2
	v_fma_f32 v124, v14, s18, v2
	v_fma_f32 v125, v15, s18, v2
	v_fma_f32 v122, v12, s18, v2
	v_fma_f32 v123, v13, s18, v2
	v_fma_f32 v120, v10, s18, v2
	v_fma_f32 v121, v11, s18, v2
	v_fma_f32 v118, v8, s18, v2
	v_fma_f32 v119, v9, s18, v2
	v_fma_f32 v116, v6, s18, v2
	v_fma_f32 v117, v7, s18, v2
	v_fma_f32 v114, v4, s18, v2
	v_fma_f32 v115, v5, s18, v2
	s_cmp_lt_i32 s48, 3
	s_waitcnt lgkmcnt(0)
	s_barrier
	s_cbranch_scc1 .LBB3_31
	s_add_i32 s0, s47, s51
	v_mov_b32_e32 v220, 0
	v_add_u32_e32 v221, s0, v215
	s_movk_i32 s14, 0xbf
	s_mov_b32 s51, 2
	v_mov_b32_e32 v18, 0
	v_mov_b32_e32 v19, v220
	v_mov_b32_e32 v20, v220
	v_mov_b32_e32 v21, v220
	v_mov_b32_e32 v22, v220
	v_mov_b32_e32 v23, v220
	v_mov_b32_e32 v24, v220
	v_mov_b32_e32 v25, v220
	v_mov_b32_e32 v26, v220
	v_mov_b32_e32 v27, v220
	v_mov_b32_e32 v28, v220
	v_mov_b32_e32 v29, v220
	v_mov_b32_e32 v30, v220
	v_mov_b32_e32 v31, v220
	v_mov_b32_e32 v32, v220
	v_mov_b32_e32 v33, v220
	v_mov_b32_e32 v34, 0
	v_mov_b32_e32 v35, v220
	v_mov_b32_e32 v36, v220
	v_mov_b32_e32 v37, v220
	v_mov_b32_e32 v38, v220
	v_mov_b32_e32 v39, v220
	v_mov_b32_e32 v40, v220
	v_mov_b32_e32 v41, v220
	v_mov_b32_e32 v42, v220
	v_mov_b32_e32 v43, v220
	v_mov_b32_e32 v44, v220
	v_mov_b32_e32 v45, v220
	v_mov_b32_e32 v46, v220
	v_mov_b32_e32 v47, v220
	v_mov_b32_e32 v48, v220
	v_mov_b32_e32 v49, v220
	v_mov_b32_e32 v50, 0
	v_mov_b32_e32 v51, v220
	v_mov_b32_e32 v52, v220
	v_mov_b32_e32 v53, v220
	v_mov_b32_e32 v54, v220
	v_mov_b32_e32 v55, v220
	v_mov_b32_e32 v56, v220
	v_mov_b32_e32 v57, v220
	v_mov_b32_e32 v58, v220
	v_mov_b32_e32 v59, v220
	v_mov_b32_e32 v60, v220
	v_mov_b32_e32 v61, v220
	v_mov_b32_e32 v62, v220
	v_mov_b32_e32 v63, v220
	v_mov_b32_e32 v64, v220
	v_mov_b32_e32 v65, v220
	v_mov_b32_e32 v66, 0
	v_mov_b32_e32 v67, v220
	v_mov_b32_e32 v68, v220
	v_mov_b32_e32 v69, v220
	v_mov_b32_e32 v70, v220
	v_mov_b32_e32 v71, v220
	v_mov_b32_e32 v72, v220
	v_mov_b32_e32 v73, v220
	v_mov_b32_e32 v74, v220
	v_mov_b32_e32 v75, v220
	v_mov_b32_e32 v76, v220
	v_mov_b32_e32 v77, v220
	v_mov_b32_e32 v78, v220
	v_mov_b32_e32 v79, v220
	v_mov_b32_e32 v80, v220
	v_mov_b32_e32 v81, v220
	s_branch .LBB3_19
.LBB3_18:
	s_cmp_ge_u32 s46, 0x100
	s_cbranch_scc1 .Lst_b1
	v_mul_f32_e32 v6, 0xbe0293ee, v194
	v_mov_b32_e32 v195, v6
	s_addk_i32 s14, 0x80
	v_fmamk_f32 v5, v130, 0x3e0293ee, v6
	v_fmamk_f32 v7, v131, 0x3e0293ee, v6
	v_fmamk_f32 v8, v132, 0x3e0293ee, v6
	v_fmamk_f32 v9, v133, 0x3e0293ee, v6
	v_fmamk_f32 v10, v134, 0x3e0293ee, v6
	v_fmamk_f32 v11, v135, 0x3e0293ee, v6
	v_fmamk_f32 v12, v136, 0x3e0293ee, v6
	v_fmamk_f32 v13, v137, 0x3e0293ee, v6
	v_fmamk_f32 v14, v138, 0x3e0293ee, v6
	v_fmamk_f32 v15, v139, 0x3e0293ee, v6
	v_fmamk_f32 v16, v140, 0x3e0293ee, v6
	v_fmamk_f32 v17, v141, 0x3e0293ee, v6
	v_fmamk_f32 v130, v142, 0x3e0293ee, v6
	v_fmamk_f32 v132, v143, 0x3e0293ee, v6
	v_fmamk_f32 v135, v144, 0x3e0293ee, v6
	v_fmac_f32_e32 v195, 0x3e0293ee, v145
	s_add_u32 s30, s30, 0x8000
	v_exp_f32_e32 v143, v5
	v_exp_f32_e32 v145, v7
	v_exp_f32_e32 v141, v8
	v_exp_f32_e32 v144, v9
	v_exp_f32_e32 v140, v10
	v_exp_f32_e32 v142, v11
	v_exp_f32_e32 v138, v12
	v_exp_f32_e32 v139, v13
	v_exp_f32_e32 v133, v14
	v_exp_f32_e32 v136, v15
	v_exp_f32_e32 v131, v16
	v_exp_f32_e32 v134, v17
	v_exp_f32_e32 v130, v130
	v_exp_f32_e32 v137, v132
	v_exp_f32_e32 v132, v135
	v_exp_f32_e32 v135, v195
	s_addc_u32 s31, s31, 0
	v_add_f32_e32 v5, v222, v223
	s_add_u32 s28, s28, 0x8000
	v_fmac_f32_e32 v5, v219, v220
	v_add_f32_e32 v220, v224, v225
	s_addc_u32 s29, s29, 0
	s_add_i32 s51, s51, 2
	v_fma_f32 v128, v128, s18, v6
	v_fma_f32 v129, v129, s18, v6
	v_fma_f32 v126, v126, s18, v6
	v_fma_f32 v127, v127, s18, v6
	v_fma_f32 v124, v124, s18, v6
	v_fma_f32 v125, v125, s18, v6
	v_fma_f32 v122, v122, s18, v6
	v_fma_f32 v123, v123, s18, v6
	v_fma_f32 v120, v120, s18, v6
	v_fma_f32 v121, v121, s18, v6
	v_fma_f32 v118, v118, s18, v6
	v_fma_f32 v119, v119, s18, v6
	v_fma_f32 v116, v116, s18, v6
	v_fma_f32 v117, v117, s18, v6
	v_fma_f32 v114, v114, s18, v6
	v_fma_f32 v115, v115, s18, v6
	v_fmac_f32_e32 v220, v5, v2
	s_cmp_ge_i32 s51, s48
	v_add_u32_e32 v221, 0xffffff80, v221
	v_mov_b32_e32 v219, v4
	s_waitcnt lgkmcnt(0)
	s_barrier
	s_branch .Lst_b2
.Lst_b1:
	s_waitcnt lgkmcnt(0)
	s_barrier
	v_mul_f32_e32 v6, 0xbe0293ee, v194
	v_mov_b32_e32 v195, v6
	s_addk_i32 s14, 0x80
	v_fmamk_f32 v5, v130, 0x3e0293ee, v6
	v_fmamk_f32 v7, v131, 0x3e0293ee, v6
	v_fmamk_f32 v8, v132, 0x3e0293ee, v6
	v_fmamk_f32 v9, v133, 0x3e0293ee, v6
	v_fmamk_f32 v10, v134, 0x3e0293ee, v6
	v_fmamk_f32 v11, v135, 0x3e0293ee, v6
	v_fmamk_f32 v12, v136, 0x3e0293ee, v6
	v_fmamk_f32 v13, v137, 0x3e0293ee, v6
	v_fmamk_f32 v14, v138, 0x3e0293ee, v6
	v_fmamk_f32 v15, v139, 0x3e0293ee, v6
	v_fmamk_f32 v16, v140, 0x3e0293ee, v6
	v_fmamk_f32 v17, v141, 0x3e0293ee, v6
	v_fmamk_f32 v130, v142, 0x3e0293ee, v6
	v_fmamk_f32 v132, v143, 0x3e0293ee, v6
	v_fmamk_f32 v135, v144, 0x3e0293ee, v6
	v_fmac_f32_e32 v195, 0x3e0293ee, v145
	s_add_u32 s30, s30, 0x8000
	v_exp_f32_e32 v143, v5
	v_exp_f32_e32 v145, v7
	v_exp_f32_e32 v141, v8
	v_exp_f32_e32 v144, v9
	v_exp_f32_e32 v140, v10
	v_exp_f32_e32 v142, v11
	v_exp_f32_e32 v138, v12
	v_exp_f32_e32 v139, v13
	v_exp_f32_e32 v133, v14
	v_exp_f32_e32 v136, v15
	v_exp_f32_e32 v131, v16
	v_exp_f32_e32 v134, v17
	v_exp_f32_e32 v130, v130
	v_exp_f32_e32 v137, v132
	v_exp_f32_e32 v132, v135
	v_exp_f32_e32 v135, v195
	s_addc_u32 s31, s31, 0
	v_add_f32_e32 v5, v222, v223
	s_add_u32 s28, s28, 0x8000
	v_fmac_f32_e32 v5, v219, v220
	v_add_f32_e32 v220, v224, v225
	s_addc_u32 s29, s29, 0
	s_add_i32 s51, s51, 2
	v_fma_f32 v128, v128, s18, v6
	v_fma_f32 v129, v129, s18, v6
	v_fma_f32 v126, v126, s18, v6
	v_fma_f32 v127, v127, s18, v6
	v_fma_f32 v124, v124, s18, v6
	v_fma_f32 v125, v125, s18, v6
	v_fma_f32 v122, v122, s18, v6
	v_fma_f32 v123, v123, s18, v6
	v_fma_f32 v120, v120, s18, v6
	v_fma_f32 v121, v121, s18, v6
	v_fma_f32 v118, v118, s18, v6
	v_fma_f32 v119, v119, s18, v6
	v_fma_f32 v116, v116, s18, v6
	v_fma_f32 v117, v117, s18, v6
	v_fma_f32 v114, v114, s18, v6
	v_fma_f32 v115, v115, s18, v6
	v_fmac_f32_e32 v220, v5, v2
	s_cmp_ge_i32 s51, s48
	v_add_u32_e32 v221, 0xffffff80, v221
	v_mov_b32_e32 v219, v4
